# MLA tile loop: specialised steady-state loop bodies per wave group (loop-invariant branches and flag updates resolved), generic loop kept for first/tail tiles and fallback mode
# speedup vs baseline: 1.0079x; 1.0076x over previous
; #define ISSUE_K(t, sl) do { glds16(Kg + (long)(t) * (KSLOT / 2), (unsigned)__builtin_amdgcn_readfirstlane(kdst + (sl) * KSLOT)); \
;         if (k2) glds16(Kg + (long)(t) * (KSLOT / 2) + 4096, (unsigned)__builtin_amdgcn_readfirstlane(kdst + (sl) * KSLOT + 8192)); } while (0)
; #define ISSUE_V(t, sl) glds16(Vg + (long)(t) * 4096, (unsigned)__builtin_amdgcn_readfirstlane(vdst + (sl) * VSLOT))
; #define SFENCE() __builtin_amdgcn_sched_barrier(0)
; template <bool FOX>
; __device__ __forceinline__ void attn_unit(const Args& A, int b, int h, int qb, LAS char* shm, LAS float* dg) {
;     ...
;     const int t_end = (tw_last - t0 + 2 < nti) ? tw_last - t0 + 2 : nti;
; #pragma unroll 1
;     for (int t = 1; t < t_end; ++t) {
;         if (t == 1 && 4 < nti) ISSUE_K(t0 + 4, 0);
;         if (t + 4 < nti) ISSUE_K(t0 + t + 4, t % NS);
;         if (t + 2 < nti) ISSUE_V(t0 + t + 2, (t + 2) % NS);
;         SFENCE();
.LBB0_825:
	s_add_i32 s27, s26, 3
	s_cmp_lt_u32 s27, s94
	s_cbranch_scc0 .LBB0_828
	s_cmp_lg_u32 s98, 0
	s_cbranch_scc0 .Lmla_ss_no
	s_cmp_lg_u32 s26, s59
	s_cbranch_scc0 .Lmla_ss_no
	s_cmp_lt_i32 s89, 4
	s_cbranch_scc1 .Lmla_ss1_top
	s_branch .Lmla_ss2_top
.Lmla_ss_no:
	s_and_b32 s27, s27, 3
	s_mulk_i32 s27, 0x3000
	s_add_i32 s27, s27, s91
	s_mov_b32 m0, s27
	v_lshl_add_u64 v[4:5], v[234:235], 0, s[56:57]
	global_load_lds_dwordx4 v[234:235], off
	s_cmp_eq_u32 s92, 2
	s_cbranch_scc0 .Lmla_fast_v
	s_add_i32 m0, s27, 0x2000
	s_nop 0
	global_load_lds_dwordx4 v[4:5], off

; template <bool FOX>
; __device__ __forceinline__ void attn_unit(const Args& A, int b, int h, int qb, LAS char* shm, LAS float* dg) {
;     ...
;     for (int t = 1; t < t_end; ++t) {
;         if (t == 1 && 4 < nti) ISSUE_K(t0 + 4, 0);
;         if (t + 4 < nti) ISSUE_K(t0 + t + 4, t % NS);
;         if (t + 2 < nti) ISSUE_V(t0 + t + 2, (t + 2) % NS);
;         SFENCE();
;         { if constexpr (!FOX) { if (t0 + t == tw_last + 1) {
; #pragma unroll
;                   for (int r = 0; r < 16; ++r) negm[r] = -INFINITY;
;                   asm volatile("" : "+v"(negm)); } }
;           const lds_cptr vp = vp0 + ((t - 1) % NS) * VSLOT; float sa = 0.f, sb = 0.f;
; #pragma unroll
;           for (int g = 0; g < 2 * NQ; ++g) {
;               if (!FOX && g == 0) c0 = __builtin_amdgcn_mfma_f32_32x32x16_bf16(kf[0], qr[0], negm, 0, 0, 0);
;               else if (!FOX && g == 1) c1 = __builtin_amdgcn_mfma_f32_32x32x16_bf16(kf[1], qr[0], negm, 0, 0, 0);
;               else if (g & 1) c1 = __builtin_amdgcn_mfma_f32_32x32x16_bf16(kf[g], qr[g >> 1], c1, 0, 0, 0); else c0 = __builtin_amdgcn_mfma_f32_32x32x16_bf16(kf[g], qr[g >> 1], c0, 0, 0, 0);
;               if (g < 8) { const int i = (g >> 1) + 4 * (g & 1); vlo[i] = vtr(vp + (i >> 2) * 4096 + (i & 3) * 1024); vhi[i] = vtr(vp + (i >> 2) * 4096 + (i & 3) * 1024 + 512);
;                   if (g < 4) { sa += pp0[4 * g]; sb += pp0[4 * g + 1]; sa += pp0[4 * g + 2]; sb += pp0[4 * g + 3]; } else { sa += pp1[4 * g - 16]; sb += pp1[4 * g - 15]; sa += pp1[4 * g - 14]; sb += pp1[4 * g - 13]; }
;                   asm volatile("" : "+v"(sa), "+v"(sb)); }
;               { constexpr int G0 = FOX ? 0 : 4; if (g >= G0) { const int q = 2 * (g - G0);
; #pragma unroll
;                   for (int k = 0; k < 2; ++k) { const int w = q + k; const unsigned pkd = w < 8 ? cvt_pk_bf16(pp0[2 * w], pp0[2 * w + 1]) : cvt_pk_bf16(pp1[2 * w - 16], pp1[2 * w - 15]); pw[w >> 2][w & 3] = pkd; } } }
;               SFENCE();
;           }
;           lrun += sa + sb; }
;         MASKONLY(t);
;         float rm; ROWMAX(rm);
;         bool resc = false;
;         if (__any(rm > THR)) { const float dl = fmaxf(rm, 0.f); mhat += dl;
; #pragma unroll
;             for (int r = 0; r < 16; ++r) { c0[r] -= dl; c1[r] -= dl; }
;             if constexpr (!FOX) {
; #pragma unroll
;                 for (int r = 0; r < 16; ++r) negm[r] = -mhat;
.Lmla_ss1_top:
	s_add_i32 s27, s26, 3
	s_and_b32 s27, s27, 3
	s_mulk_i32 s27, 0x3000
	s_add_i32 s27, s27, s91
	s_mov_b32 m0, s27
	v_lshl_add_u64 v[4:5], v[234:235], 0, s[56:57]
	global_load_lds_dwordx4 v[234:235], off
	s_cmp_eq_u32 s92, 2
	s_cbranch_scc0 .Lmla_ss1_v
	s_add_i32 m0, s27, 0x2000
	s_nop 0
	global_load_lds_dwordx4 v[4:5], off
.Lmla_ss1_v:
	s_add_i32 s27, s42, 0x6000
	s_and_b32 s27, s27, 0x6000
	s_add_i32 m0, s27, s93
	v_lshl_add_u64 v[4:5], v[232:233], 0, s[42:43]
	global_load_lds_dwordx4 v[4:5], off
	s_add_i32 s27, s42, 0x8000
	v_mfma_f32_32x32x16_bf16 v[114:129], v[206:209], v[138:141], v[82:97]
	s_and_b32 s27, s27, 0x6000
	v_add_u32_e32 v3, s27, v247
	ds_read_b64_tr_b16 v[206:207], v3 offset:49152
	ds_read_b64_tr_b16 v[208:209], v3 offset:49664
	v_add_f32_e32 v4, 0, v67
	v_add_f32_e32 v5, 0, v66
	v_add_f32_e32 v4, v69, v4
	v_add_f32_e32 v5, v68, v5
	v_mfma_f32_32x32x16_bf16 v[98:113], v[194:197], v[138:141], v[82:97]
	ds_read_b64_tr_b16 v[194:195], v3 offset:53248
	ds_read_b64_tr_b16 v[196:197], v3 offset:53760
	v_add_f32_e32 v4, v71, v4
	v_add_f32_e32 v5, v70, v5
	v_add_f32_e32 v4, v73, v4
	v_add_f32_e32 v5, v72, v5
	v_mfma_f32_32x32x16_bf16 v[114:129], v[202:205], v[142:145], v[114:129]
	ds_read_b64_tr_b16 v[202:203], v3 offset:50176
	ds_read_b64_tr_b16 v[204:205], v3 offset:50688
	v_add_f32_e32 v4, v75, v4
	v_add_f32_e32 v5, v74, v5
	v_add_f32_e32 v4, v77, v4
	v_add_f32_e32 v5, v76, v5
	v_mfma_f32_32x32x16_bf16 v[98:113], v[186:189], v[142:145], v[98:113]
	ds_read_b64_tr_b16 v[214:215], v3 offset:54272
	ds_read_b64_tr_b16 v[216:217], v3 offset:54784
	v_add_f32_e32 v4, v79, v4
	v_add_f32_e32 v5, v78, v5
	v_add_f32_e32 v4, v81, v4
	v_add_f32_e32 v5, v80, v5
	v_mfma_f32_32x32x16_bf16 v[114:129], v[198:201], v[146:149], v[114:129]
	ds_read_b64_tr_b16 v[210:211], v3 offset:51200
	ds_read_b64_tr_b16 v[212:213], v3 offset:51712
	v_add_f32_e32 v4, v51, v4
	v_add_f32_e32 v5, v50, v5
	v_add_f32_e32 v4, v53, v4
	v_add_f32_e32 v5, v52, v5
	v_mfma_f32_32x32x16_bf16 v[98:113], v[182:185], v[146:149], v[98:113]
	ds_read_b64_tr_b16 v[12:13], v3 offset:55296
	ds_read_b64_tr_b16 v[14:15], v3 offset:55808
	v_add_f32_e32 v4, v55, v4
	v_add_f32_e32 v5, v54, v5
	v_add_f32_e32 v4, v57, v4
	v_add_f32_e32 v5, v56, v5
	v_mfma_f32_32x32x16_bf16 v[114:129], v[190:193], v[150:153], v[114:129]
	ds_read_b64_tr_b16 v[8:9], v3 offset:52224
	ds_read_b64_tr_b16 v[10:11], v3 offset:52736
	v_add_f32_e32 v4, v59, v4
	v_add_f32_e32 v16, v61, v4
	v_add_f32_e32 v4, v58, v5
	v_add_f32_e32 v17, v60, v4
	v_mfma_f32_32x32x16_bf16 v[98:113], v[170:173], v[150:153], v[98:113]
	ds_read_b64_tr_b16 v[4:5], v3 offset:56320
	ds_read_b64_tr_b16 v[6:7], v3 offset:56832
	v_add_f32_e32 v3, v63, v16
	v_add_f32_e32 v16, v62, v17
	v_add_f32_e32 v3, v65, v3
	v_add_f32_e32 v16, v64, v16
	v_mfma_f32_32x32x16_bf16 v[114:129], v[178:181], v[154:157], v[114:129]
	v_cvt_pk_bf16_f32 v178, v50, v51
	v_cvt_pk_bf16_f32 v179, v52, v53
	v_cvt_pk_bf16_f32 v186, v66, v67
	v_cvt_pk_bf16_f32 v187, v68, v69
	v_mfma_f32_32x32x16_bf16 v[98:113], v[166:169], v[154:157], v[98:113]
	v_cvt_pk_bf16_f32 v180, v54, v55
	v_cvt_pk_bf16_f32 v181, v56, v57
	v_cvt_pk_bf16_f32 v188, v70, v71
	v_cvt_pk_bf16_f32 v189, v72, v73
	v_mfma_f32_32x32x16_bf16 v[114:129], v[174:177], v[158:161], v[114:129]
	v_cvt_pk_bf16_f32 v218, v58, v59
	v_cvt_pk_bf16_f32 v219, v60, v61
	v_cvt_pk_bf16_f32 v182, v74, v75
	v_cvt_pk_bf16_f32 v183, v76, v77
	v_mfma_f32_32x32x16_bf16 v[98:113], v[162:165], v[158:161], v[98:113]
	v_cvt_pk_bf16_f32 v220, v62, v63
	v_cvt_pk_bf16_f32 v221, v64, v65
	v_cvt_pk_bf16_f32 v184, v78, v79
	v_cvt_pk_bf16_f32 v185, v80, v81
	v_add_f32_e32 v3, v3, v16
	v_add_f32_e32 v246, v246, v3
	s_nop 3
	s_waitcnt lgkmcnt(0)
	v_mfma_f32_32x32x16_bf16 v[18:33], v[186:189], v[206:209], v[18:33]
	s_add_i32 s27, s26, 1
	s_and_b32 s64, s27, 3
	s_mulk_i32 s64, 0x3000
	v_exp_f32_e32 v66, v114
	v_exp_f32_e32 v67, v115
	v_exp_f32_e32 v68, v116
	v_exp_f32_e32 v69, v117
	v_add_u32_e32 v3, s64, v248
	v_mfma_f32_32x32x16_bf16 v[34:49], v[186:189], v[194:197], v[34:49]
	v_exp_f32_e32 v70, v118
	v_exp_f32_e32 v71, v119
	v_exp_f32_e32 v72, v120
	v_exp_f32_e32 v73, v121
	ds_read_b128 v[206:209], v3
	ds_read_b128 v[194:197], v3 offset:512
	v_mfma_f32_32x32x16_bf16 v[18:33], v[182:185], v[202:205], v[18:33]
	v_exp_f32_e32 v74, v122
	v_exp_f32_e32 v75, v123
	v_exp_f32_e32 v76, v124
	v_exp_f32_e32 v77, v125
	ds_read_b128 v[202:205], v3 offset:2048
	ds_read_b128 v[186:189], v3 offset:2560
	v_mfma_f32_32x32x16_bf16 v[34:49], v[182:185], v[214:217], v[34:49]
	v_exp_f32_e32 v78, v126
	v_exp_f32_e32 v79, v127
	v_exp_f32_e32 v80, v128
	v_exp_f32_e32 v81, v129
	ds_read_b128 v[198:201], v3 offset:4096
	ds_read_b128 v[182:185], v3 offset:4608
	v_mfma_f32_32x32x16_bf16 v[18:33], v[178:181], v[210:213], v[18:33]
	v_exp_f32_e32 v50, v98
	v_exp_f32_e32 v51, v99
	v_exp_f32_e32 v52, v100
	v_exp_f32_e32 v53, v101
	ds_read_b128 v[190:193], v3 offset:6144
	ds_read_b128 v[170:173], v3 offset:6656
	v_mfma_f32_32x32x16_bf16 v[34:49], v[178:181], v[12:15], v[34:49]
	v_exp_f32_e32 v54, v102
	v_exp_f32_e32 v55, v103
	v_exp_f32_e32 v56, v104
	v_exp_f32_e32 v57, v105
	ds_read_b128 v[178:181], v3 offset:8192
	ds_read_b128 v[166:169], v3 offset:8704
	v_mfma_f32_32x32x16_bf16 v[18:33], v[218:221], v[8:11], v[18:33]
	v_exp_f32_e32 v58, v106
	v_exp_f32_e32 v59, v107
	v_exp_f32_e32 v60, v108
	v_exp_f32_e32 v61, v109
	ds_read_b128 v[174:177], v3 offset:10240
	ds_read_b128 v[162:165], v3 offset:10752
	v_mfma_f32_32x32x16_bf16 v[34:49], v[218:221], v[4:7], v[34:49]
	v_exp_f32_e32 v62, v110
	v_exp_f32_e32 v63, v111
	v_exp_f32_e32 v64, v112
	v_exp_f32_e32 v65, v113
	s_waitcnt vmcnt(4)
	s_waitcnt lgkmcnt(0)
	s_barrier
	s_add_u32 s42, s42, 0x2000
	s_addc_u32 s43, s43, 0
	v_lshl_add_u64 v[234:235], v[234:235], 0, s[62:63]
	s_cmp_eq_u32 s27, s96
	s_cbranch_scc1 .Lmla_ss_done
	s_mov_b32 s26, s27
	s_add_i32 s64, s26, 3
	s_cmp_lt_u32 s64, s94
	s_cbranch_scc1 .Lmla_ss1_top
	s_branch .Lmla_ss_back

; template <bool FOX>
; __device__ __forceinline__ void attn_unit(const Args& A, int b, int h, int qb, LAS char* shm, LAS float* dg) {
;     ...
;     for (int t = 1; t < t_end; ++t) {
;         if (t == 1 && 4 < nti) ISSUE_K(t0 + 4, 0);
;         if (t + 4 < nti) ISSUE_K(t0 + t + 4, t % NS);
;         if (t + 2 < nti) ISSUE_V(t0 + t + 2, (t + 2) % NS);
;         SFENCE();
;         { if constexpr (!FOX) { if (t0 + t == tw_last + 1) {
; #pragma unroll
;                   for (int r = 0; r < 16; ++r) negm[r] = -INFINITY;
;                   asm volatile("" : "+v"(negm)); } }
;           const lds_cptr vp = vp0 + ((t - 1) % NS) * VSLOT; float sa = 0.f, sb = 0.f;
; #pragma unroll
;           for (int g = 0; g < 2 * NQ; ++g) {
;               if (!FOX && g == 0) c0 = __builtin_amdgcn_mfma_f32_32x32x16_bf16(kf[0], qr[0], negm, 0, 0, 0);
;               else if (!FOX && g == 1) c1 = __builtin_amdgcn_mfma_f32_32x32x16_bf16(kf[1], qr[0], negm, 0, 0, 0);
;               else if (g & 1) c1 = __builtin_amdgcn_mfma_f32_32x32x16_bf16(kf[g], qr[g >> 1], c1, 0, 0, 0); else c0 = __builtin_amdgcn_mfma_f32_32x32x16_bf16(kf[g], qr[g >> 1], c0, 0, 0, 0);
;               if (g < 8) { const int i = (g >> 1) + 4 * (g & 1); vlo[i] = vtr(vp + (i >> 2) * 4096 + (i & 3) * 1024); vhi[i] = vtr(vp + (i >> 2) * 4096 + (i & 3) * 1024 + 512);
;                   if (g < 4) { sa += pp0[4 * g]; sb += pp0[4 * g + 1]; sa += pp0[4 * g + 2]; sb += pp0[4 * g + 3]; } else { sa += pp1[4 * g - 16]; sb += pp1[4 * g - 15]; sa += pp1[4 * g - 14]; sb += pp1[4 * g - 13]; }
;                   asm volatile("" : "+v"(sa), "+v"(sb)); }
;               { constexpr int G0 = FOX ? 0 : 4; if (g >= G0) { const int q = 2 * (g - G0);
; #pragma unroll
;                   for (int k = 0; k < 2; ++k) { const int w = q + k; const unsigned pkd = w < 8 ? cvt_pk_bf16(pp0[2 * w], pp0[2 * w + 1]) : cvt_pk_bf16(pp1[2 * w - 16], pp1[2 * w - 15]); pw[w >> 2][w & 3] = pkd; } } }
;               SFENCE();
;           }
;           lrun += sa + sb; }
;         MASKONLY(t);
;         float rm; ROWMAX(rm);
;         bool resc = false;
;         if (__any(rm > THR)) { const float dl = fmaxf(rm, 0.f); mhat += dl;
; #pragma unroll
;             for (int r = 0; r < 16; ++r) { c0[r] -= dl; c1[r] -= dl; }
;             if constexpr (!FOX) {
; #pragma unroll
;                 for (int r = 0; r < 16; ++r) negm[r] = -mhat;
.Lmla_ss2_v:
	s_add_i32 s27, s42, 0x6000
	s_and_b32 s27, s27, 0x6000
	s_add_i32 m0, s27, s93
	v_lshl_add_u64 v[4:5], v[232:233], 0, s[42:43]
	global_load_lds_dwordx4 v[4:5], off
	s_add_i32 s27, s42, 0x8000
	v_mfma_f32_32x32x16_bf16 v[114:129], v[206:209], v[138:141], v[82:97]
	s_and_b32 s27, s27, 0x6000
	v_add_u32_e32 v3, s27, v247
	ds_read_b64_tr_b16 v[206:207], v3 offset:49152
	ds_read_b64_tr_b16 v[208:209], v3 offset:49664
	v_add_f32_e32 v4, 0, v67
	v_add_f32_e32 v5, 0, v66
	v_add_f32_e32 v4, v69, v4
	v_add_f32_e32 v5, v68, v5
	v_mfma_f32_32x32x16_bf16 v[98:113], v[194:197], v[138:141], v[82:97]
	ds_read_b64_tr_b16 v[194:195], v3 offset:53248
	ds_read_b64_tr_b16 v[196:197], v3 offset:53760
	v_add_f32_e32 v4, v71, v4
	v_add_f32_e32 v5, v70, v5
	v_add_f32_e32 v4, v73, v4
	v_add_f32_e32 v5, v72, v5
	v_mfma_f32_32x32x16_bf16 v[114:129], v[202:205], v[142:145], v[114:129]
	ds_read_b64_tr_b16 v[202:203], v3 offset:50176
	ds_read_b64_tr_b16 v[204:205], v3 offset:50688
	v_add_f32_e32 v4, v75, v4
	v_add_f32_e32 v5, v74, v5
	v_add_f32_e32 v4, v77, v4
	v_add_f32_e32 v5, v76, v5
	v_mfma_f32_32x32x16_bf16 v[98:113], v[186:189], v[142:145], v[98:113]
	ds_read_b64_tr_b16 v[214:215], v3 offset:54272
	ds_read_b64_tr_b16 v[216:217], v3 offset:54784
	v_add_f32_e32 v4, v79, v4
	v_add_f32_e32 v5, v78, v5
	v_add_f32_e32 v4, v81, v4
	v_add_f32_e32 v5, v80, v5
	v_mfma_f32_32x32x16_bf16 v[114:129], v[198:201], v[146:149], v[114:129]
	ds_read_b64_tr_b16 v[210:211], v3 offset:51200
	ds_read_b64_tr_b16 v[212:213], v3 offset:51712
	v_add_f32_e32 v4, v51, v4
	v_add_f32_e32 v5, v50, v5
	v_add_f32_e32 v4, v53, v4
	v_add_f32_e32 v5, v52, v5
	v_mfma_f32_32x32x16_bf16 v[98:113], v[182:185], v[146:149], v[98:113]
	ds_read_b64_tr_b16 v[12:13], v3 offset:55296
	ds_read_b64_tr_b16 v[14:15], v3 offset:55808
	v_add_f32_e32 v4, v55, v4
	v_add_f32_e32 v5, v54, v5
	v_add_f32_e32 v4, v57, v4
	v_add_f32_e32 v5, v56, v5
	v_mfma_f32_32x32x16_bf16 v[114:129], v[190:193], v[150:153], v[114:129]
	ds_read_b64_tr_b16 v[8:9], v3 offset:52224
	ds_read_b64_tr_b16 v[10:11], v3 offset:52736
	v_add_f32_e32 v4, v59, v4
	v_add_f32_e32 v16, v61, v4
	v_add_f32_e32 v4, v58, v5
	v_add_f32_e32 v17, v60, v4
	v_mfma_f32_32x32x16_bf16 v[98:113], v[170:173], v[150:153], v[98:113]
	ds_read_b64_tr_b16 v[4:5], v3 offset:56320
	ds_read_b64_tr_b16 v[6:7], v3 offset:56832
	v_add_f32_e32 v3, v63, v16
	v_add_f32_e32 v16, v62, v17
	v_add_f32_e32 v3, v65, v3
	v_add_f32_e32 v16, v64, v16
	v_mfma_f32_32x32x16_bf16 v[114:129], v[178:181], v[154:157], v[114:129]
	v_cvt_pk_bf16_f32 v178, v50, v51
	v_cvt_pk_bf16_f32 v179, v52, v53
	v_cvt_pk_bf16_f32 v186, v66, v67
	v_cvt_pk_bf16_f32 v187, v68, v69
	v_mfma_f32_32x32x16_bf16 v[98:113], v[166:169], v[154:157], v[98:113]
	v_cvt_pk_bf16_f32 v180, v54, v55
	v_cvt_pk_bf16_f32 v181, v56, v57
	v_cvt_pk_bf16_f32 v188, v70, v71
	v_cvt_pk_bf16_f32 v189, v72, v73
	v_mfma_f32_32x32x16_bf16 v[114:129], v[174:177], v[158:161], v[114:129]
	v_cvt_pk_bf16_f32 v218, v58, v59
	v_cvt_pk_bf16_f32 v219, v60, v61
	v_cvt_pk_bf16_f32 v182, v74, v75
	v_cvt_pk_bf16_f32 v183, v76, v77
	v_mfma_f32_32x32x16_bf16 v[98:113], v[162:165], v[158:161], v[98:113]
	v_cvt_pk_bf16_f32 v220, v62, v63
	v_cvt_pk_bf16_f32 v221, v64, v65
	v_cvt_pk_bf16_f32 v184, v78, v79
	v_cvt_pk_bf16_f32 v185, v80, v81
	v_add_f32_e32 v3, v3, v16
	v_add_f32_e32 v246, v246, v3
	s_waitcnt vmcnt(3)
	s_waitcnt lgkmcnt(0)
	s_barrier
	v_mfma_f32_32x32x16_bf16 v[18:33], v[186:189], v[206:209], v[18:33]
	s_add_i32 s27, s26, 1
	s_and_b32 s64, s27, 3
	s_mulk_i32 s64, 0x3000
	v_exp_f32_e32 v66, v114
	v_exp_f32_e32 v67, v115
	v_exp_f32_e32 v68, v116
	v_exp_f32_e32 v69, v117
	v_add_u32_e32 v3, s64, v248
	v_mfma_f32_32x32x16_bf16 v[34:49], v[186:189], v[194:197], v[34:49]
	v_exp_f32_e32 v70, v118
	v_exp_f32_e32 v71, v119
	v_exp_f32_e32 v72, v120
	v_exp_f32_e32 v73, v121
	ds_read_b128 v[206:209], v3
	ds_read_b128 v[194:197], v3 offset:512
	v_mfma_f32_32x32x16_bf16 v[18:33], v[182:185], v[202:205], v[18:33]
	v_exp_f32_e32 v74, v122
	v_exp_f32_e32 v75, v123
	v_exp_f32_e32 v76, v124
	v_exp_f32_e32 v77, v125
	ds_read_b128 v[202:205], v3 offset:2048
	ds_read_b128 v[186:189], v3 offset:2560
	v_mfma_f32_32x32x16_bf16 v[34:49], v[182:185], v[214:217], v[34:49]
	v_exp_f32_e32 v78, v126
	v_exp_f32_e32 v79, v127
	v_exp_f32_e32 v80, v128
	v_exp_f32_e32 v81, v129
	ds_read_b128 v[198:201], v3 offset:4096
	ds_read_b128 v[182:185], v3 offset:4608
	v_mfma_f32_32x32x16_bf16 v[18:33], v[178:181], v[210:213], v[18:33]
	v_exp_f32_e32 v50, v98
	v_exp_f32_e32 v51, v99
	v_exp_f32_e32 v52, v100
	v_exp_f32_e32 v53, v101
	ds_read_b128 v[190:193], v3 offset:6144
	ds_read_b128 v[170:173], v3 offset:6656
	v_mfma_f32_32x32x16_bf16 v[34:49], v[178:181], v[12:15], v[34:49]
	v_exp_f32_e32 v54, v102
	v_exp_f32_e32 v55, v103
	v_exp_f32_e32 v56, v104
	v_exp_f32_e32 v57, v105
	ds_read_b128 v[178:181], v3 offset:8192
	ds_read_b128 v[166:169], v3 offset:8704
	v_mfma_f32_32x32x16_bf16 v[18:33], v[218:221], v[8:11], v[18:33]
	v_exp_f32_e32 v58, v106
	v_exp_f32_e32 v59, v107
	v_exp_f32_e32 v60, v108
	v_exp_f32_e32 v61, v109
	ds_read_b128 v[174:177], v3 offset:10240
	ds_read_b128 v[162:165], v3 offset:10752
	v_mfma_f32_32x32x16_bf16 v[34:49], v[218:221], v[4:7], v[34:49]
	v_exp_f32_e32 v62, v110
	v_exp_f32_e32 v63, v111
	v_exp_f32_e32 v64, v112
	v_exp_f32_e32 v65, v113
	s_waitcnt lgkmcnt(0)
	s_add_u32 s42, s42, 0x2000
	s_addc_u32 s43, s43, 0
	v_lshl_add_u64 v[234:235], v[234:235], 0, s[62:63]
	s_cmp_eq_u32 s27, s96
	s_cbranch_scc1 .Lmla_ss_done
	s_mov_b32 s26, s27
	s_add_i32 s64, s26, 3
	s_cmp_lt_u32 s64, s94
	s_cbranch_scc1 .Lmla_ss2_top
	s_branch .Lmla_ss_back
.Lmla_ss_back:
	s_mov_b64 s[60:61], 0
	s_branch .LBB0_825
.Lmla_ss_done:
	s_mov_b64 s[46:47], -1
	s_mov_b64 s[52:53], -1
	s_mov_b64 s[60:61], 0
	s_branch .LBB0_867
